# merged the 7 per-k-step waits of the layer-1 loop into one vmcnt+lgkmcnt wait per step
# baseline (speedup 1.0000x reference)
.LBB1_4:
	s_waitcnt lgkmcnt(0)
	s_and_saveexec_b64 s[8:9], s[2:3]
	v_perm_b32 v5, v1, v248, s23
	v_perm_b32 v9, v121, v249, s23
	v_perm_b32 v17, v144, v250, s23
	v_perm_b32 v29, v145, v251, s23
	s_or_b64 exec, exec, s[8:9]
	v_add_u32_e32 v0, 0x12c00, v105
	ds_read_b128 v[240:243], v0
	ds_read_b128 v[244:247], v0 offset:16
	ds_read_b128 v[248:251], v0 offset:32
	ds_read_b128 v[252:255], v0 offset:48
	v_mfma_f32_16x16x32_f16 v[126:129], v[30:33], v[6:9], 0
	s_cmp_lg_u32 s22, 0x818000
	v_mfma_f32_16x16x32_f16 v[122:125], v[30:33], v[2:5], 0
	s_cselect_b32 s9, s11, 15
	s_nop 2
	v_cvt_pk_f16_f32 v121, v126, v127
	v_cvt_pk_f16_f32 v127, v128, v129
	v_mfma_f32_16x16x32_f16 v[134:137], v[30:33], v[14:17], 0
	v_pk_max_f16 v126, v121, 0
	s_nop 0
	v_cvt_pk_f16_f32 v0, v122, v123
	v_cvt_pk_f16_f32 v1, v124, v125
	v_mfma_f32_16x16x32_f16 v[30:33], v[30:33], v[26:29], 0
	v_pk_max_f16 v127, v127, 0
	v_pk_max_f16 v0, v0, 0
	v_pk_max_f16 v1, v1, 0
	v_mfma_f32_16x16x32_f16 v[122:125], v[22:25], v[2:5], 0
	ds_write2st64_b64 v107, v[0:1], v[126:127] offset1:32
	s_nop 1
	v_cvt_pk_f16_f32 v0, v134, v135
	v_cvt_pk_f16_f32 v1, v136, v137
	v_mfma_f32_16x16x32_f16 v[126:129], v[22:25], v[6:9], 0
	s_nop 0
	v_cvt_pk_f16_f32 v30, v30, v31
	v_cvt_pk_f16_f32 v31, v32, v33
	v_pk_max_f16 v0, v0, 0
	v_mfma_f32_16x16x32_f16 v[134:137], v[22:25], v[14:17], 0
	v_pk_max_f16 v30, v30, 0
	v_pk_max_f16 v31, v31, 0
	v_pk_max_f16 v1, v1, 0
	v_mfma_f32_16x16x32_f16 v[22:25], v[22:25], v[26:29], 0
	ds_write2st64_b64 v107, v[0:1], v[30:31] offset0:64 offset1:96
	v_cvt_pk_f16_f32 v0, v122, v123
	v_cvt_pk_f16_f32 v1, v124, v125
	v_mfma_f32_16x16x32_f16 v[30:33], v[18:21], v[2:5], 0
	v_pk_max_f16 v0, v0, 0
	v_cvt_pk_f16_f32 v139, v128, v129
	v_pk_max_f16 v1, v1, 0
	v_mfma_f32_16x16x32_f16 v[122:125], v[18:21], v[6:9], 0
	v_cvt_pk_f16_f32 v121, v126, v127
	v_pk_max_f16 v138, v121, 0
	v_pk_max_f16 v139, v139, 0
	v_mfma_f32_16x16x32_f16 v[126:129], v[18:21], v[14:17], 0
	ds_write2st64_b64 v108, v[0:1], v[138:139] offset1:32
	v_cvt_pk_f16_f32 v0, v134, v135
	v_cvt_pk_f16_f32 v1, v136, v137
	v_mfma_f32_16x16x32_f16 v[18:21], v[18:21], v[26:29], 0
	v_pk_max_f16 v0, v0, 0
	v_cvt_pk_f16_f32 v139, v24, v25
	v_pk_max_f16 v1, v1, 0
	v_mfma_f32_16x16x32_f16 v[134:137], v[10:13], v[2:5], 0
	v_cvt_pk_f16_f32 v121, v22, v23
	v_pk_max_f16 v138, v121, 0
	v_pk_max_f16 v139, v139, 0
	ds_write2st64_b64 v108, v[0:1], v[138:139] offset0:64 offset1:96
	v_cvt_pk_f16_f32 v0, v30, v31
	v_mfma_f32_16x16x32_f16 v[22:25], v[10:13], v[6:9], 0
	v_cvt_pk_f16_f32 v1, v32, v33
	v_pk_max_f16 v0, v0, 0
	v_cvt_pk_f16_f32 v30, v122, v123
	v_cvt_pk_f16_f32 v31, v124, v125
	v_mfma_f32_16x16x32_f16 v[138:141], v[10:13], v[14:17], 0
	v_pk_max_f16 v1, v1, 0
	v_pk_max_f16 v30, v30, 0
	v_pk_max_f16 v31, v31, 0
	ds_write2st64_b64 v109, v[0:1], v[30:31] offset1:32
	v_cvt_pk_f16_f32 v0, v126, v127
	v_mfma_f32_16x16x32_f16 v[10:13], v[10:13], v[26:29], 0
	v_cvt_pk_f16_f32 v1, v128, v129
	v_pk_max_f16 v0, v0, 0
	v_cvt_pk_f16_f32 v18, v18, v19
	v_cvt_pk_f16_f32 v19, v20, v21
	v_pk_max_f16 v1, v1, 0
	v_pk_max_f16 v18, v18, 0
	v_pk_max_f16 v19, v19, 0
	ds_write2st64_b64 v109, v[0:1], v[18:19] offset0:64 offset1:96
	v_cvt_pk_f16_f32 v0, v134, v135
	v_cvt_pk_f16_f32 v1, v136, v137
	v_pk_max_f16 v0, v0, 0
	v_cvt_pk_f16_f32 v18, v22, v23
	v_cvt_pk_f16_f32 v19, v24, v25
	v_pk_max_f16 v1, v1, 0
	v_pk_max_f16 v18, v18, 0
	v_pk_max_f16 v19, v19, 0
	ds_write2st64_b64 v110, v[0:1], v[18:19] offset1:32
	v_cvt_pk_f16_f32 v0, v138, v139
	v_cvt_pk_f16_f32 v1, v140, v141
	v_pk_max_f16 v0, v0, 0
	v_cvt_pk_f16_f32 v10, v10, v11
	v_cvt_pk_f16_f32 v11, v12, v13
	v_pk_max_f16 v1, v1, 0
	v_pk_max_f16 v10, v10, 0
	v_pk_max_f16 v11, v11, 0
	ds_write2st64_b64 v110, v[0:1], v[10:11] offset0:64 offset1:96
	s_waitcnt lgkmcnt(0)
	s_barrier
	ds_read_b128 v[122:125], v111
	ds_read_b128 v[126:129], v111 offset:16384
	ds_read_b128 v[134:137], v111 offset:32768
	ds_read_b128 v[138:141], v111 offset:49152
	ds_read_b128 v[142:145], v98
	ds_read_b128 v[152:155], v98 offset:16384
	ds_read_b128 v[156:159], v98 offset:32768
	ds_read_b128 v[160:163], v98 offset:49152
	s_lshl_b32 s20, s9, 7
	v_lshl_add_u64 v[0:1], s[20:21], 3, v[132:133]
	s_add_i32 s25, s22, 0xfff88000
	s_lshl_b32 s8, s9, 8
	buffer_load_dwordx4 v[192:195], v147, s[16:19], s25 offen
	buffer_load_dwordx4 v[196:199], v148, s[16:19], s25 offen
	buffer_load_dwordx4 v[200:203], v149, s[16:19], s25 offen
	buffer_load_dwordx4 v[204:207], v150, s[16:19], s25 offen
	s_waitcnt vmcnt(16) lgkmcnt(4)
	v_mfma_f32_16x16x32_f16 v[164:167], v[58:61], v[122:125], v[240:243]
	v_mfma_f32_16x16x32_f16 v[168:171], v[58:61], v[126:129], v[240:243]
	v_mfma_f32_16x16x32_f16 v[172:175], v[58:61], v[134:137], v[240:243]
	v_mfma_f32_16x16x32_f16 v[10:13], v[58:61], v[138:141], v[240:243]
	v_mfma_f32_16x16x32_f16 v[58:61], v[54:57], v[122:125], v[244:247]
	v_mfma_f32_16x16x32_f16 v[176:179], v[54:57], v[126:129], v[244:247]
	v_mfma_f32_16x16x32_f16 v[180:183], v[54:57], v[134:137], v[244:247]
	v_mfma_f32_16x16x32_f16 v[18:21], v[54:57], v[138:141], v[244:247]
	v_mfma_f32_16x16x32_f16 v[54:57], v[50:53], v[122:125], v[248:251]
	v_mfma_f32_16x16x32_f16 v[184:187], v[50:53], v[126:129], v[248:251]
	v_mfma_f32_16x16x32_f16 v[188:191], v[50:53], v[134:137], v[248:251]
	v_mfma_f32_16x16x32_f16 v[22:25], v[50:53], v[138:141], v[248:251]
	v_mfma_f32_16x16x32_f16 v[50:53], v[38:41], v[122:125], v[252:255]
	v_mfma_f32_16x16x32_f16 v[122:125], v[38:41], v[126:129], v[252:255]
	v_mfma_f32_16x16x32_f16 v[126:129], v[38:41], v[134:137], v[252:255]
	v_mfma_f32_16x16x32_f16 v[38:41], v[38:41], v[138:141], v[252:255]
	ds_read_b128 v[136:139], v99
	ds_read_b128 v[208:211], v99 offset:16384
	ds_read_b128 v[212:215], v99 offset:32768
	ds_read_b128 v[216:219], v99 offset:49152
	s_add_i32 s9, s22, 0xfff90000
	s_waitcnt vmcnt(12) lgkmcnt(4)
	v_mfma_f32_16x16x32_f16 v[164:167], v[94:97], v[142:145], v[164:167]
	v_mfma_f32_16x16x32_f16 v[168:171], v[94:97], v[152:155], v[168:171]
	v_mfma_f32_16x16x32_f16 v[58:61], v[90:93], v[142:145], v[58:61]
	v_mfma_f32_16x16x32_f16 v[176:179], v[90:93], v[152:155], v[176:179]
	v_mfma_f32_16x16x32_f16 v[54:57], v[78:81], v[142:145], v[54:57]
	v_mfma_f32_16x16x32_f16 v[184:187], v[78:81], v[152:155], v[184:187]
	v_mfma_f32_16x16x32_f16 v[50:53], v[34:37], v[142:145], v[50:53]
	buffer_load_dwordx4 v[140:143], v147, s[16:19], s9 offen
	buffer_load_dwordx4 v[220:223], v148, s[16:19], s9 offen
	v_mfma_f32_16x16x32_f16 v[122:125], v[34:37], v[152:155], v[122:125]
	buffer_load_dwordx4 v[152:155], v149, s[16:19], s9 offen
	buffer_load_dwordx4 v[224:227], v150, s[16:19], s9 offen
	s_mov_b32 s9, s21
	v_mfma_f32_16x16x32_f16 v[172:175], v[94:97], v[156:159], v[172:175]
	v_mfma_f32_16x16x32_f16 v[94:97], v[94:97], v[160:163], v[10:13]
	s_nop 2
	v_lshl_add_u64 v[10:11], s[8:9], 4, v[130:131]
	v_mfma_f32_16x16x32_f16 v[180:183], v[90:93], v[156:159], v[180:183]
	v_mfma_f32_16x16x32_f16 v[90:93], v[90:93], v[160:163], v[18:21]
	v_mfma_f32_16x16x32_f16 v[188:191], v[78:81], v[156:159], v[188:191]
	v_mfma_f32_16x16x32_f16 v[78:81], v[78:81], v[160:163], v[22:25]
	global_load_dwordx4 v[30:33], v[10:11], off
	s_nop 1
	global_load_dwordx4 v[22:25], v[10:11], off offset:1024
	global_load_dwordx4 v[18:21], v[10:11], off offset:2048
	s_nop 0
	global_load_dwordx4 v[10:13], v[10:11], off offset:3072
	s_nop 0
	global_load_dwordx2 v[134:135], v[0:1], off
	v_mfma_f32_16x16x32_f16 v[126:129], v[34:37], v[156:159], v[126:129]
	v_mfma_f32_16x16x32_f16 v[34:37], v[34:37], v[160:163], v[38:41]
	s_nop 2
	ds_read_b128 v[38:41], v100
	ds_read_b128 v[156:159], v100 offset:16384
	ds_read_b128 v[160:163], v100 offset:32768
	ds_read_b128 v[228:231], v100 offset:49152
	s_add_i32 s8, s22, 0xfff98000
	s_waitcnt vmcnt(17) lgkmcnt(4)
	v_mfma_f32_16x16x32_f16 v[164:167], v[82:85], v[136:139], v[164:167]
	v_mfma_f32_16x16x32_f16 v[168:171], v[82:85], v[208:211], v[168:171]
	v_mfma_f32_16x16x32_f16 v[172:175], v[82:85], v[212:215], v[172:175]
	v_mfma_f32_16x16x32_f16 v[82:85], v[82:85], v[216:219], v[94:97]
	v_mfma_f32_16x16x32_f16 v[58:61], v[70:73], v[136:139], v[58:61]
	v_mfma_f32_16x16x32_f16 v[94:97], v[70:73], v[208:211], v[176:179]
	v_mfma_f32_16x16x32_f16 v[176:179], v[70:73], v[212:215], v[180:183]
	v_mfma_f32_16x16x32_f16 v[70:73], v[70:73], v[216:219], v[90:93]
	v_mfma_f32_16x16x32_f16 v[54:57], v[62:65], v[136:139], v[54:57]
	v_mfma_f32_16x16x32_f16 v[90:93], v[62:65], v[208:211], v[184:187]
	v_mfma_f32_16x16x32_f16 v[180:183], v[62:65], v[212:215], v[188:191]
	v_mfma_f32_16x16x32_f16 v[62:65], v[62:65], v[216:219], v[78:81]
	v_mfma_f32_16x16x32_f16 v[50:53], v[42:45], v[136:139], v[50:53]
	v_mfma_f32_16x16x32_f16 v[78:81], v[42:45], v[208:211], v[122:125]
	v_mfma_f32_16x16x32_f16 v[122:125], v[42:45], v[212:215], v[126:129]
	s_nop 2
	buffer_load_dwordx4 v[126:129], v147, s[16:19], s8 offen
	buffer_load_dwordx4 v[136:139], v148, s[16:19], s8 offen
	buffer_load_dwordx4 v[184:187], v149, s[16:19], s8 offen
	buffer_load_dwordx4 v[188:191], v150, s[16:19], s8 offen
	v_mfma_f32_16x16x32_f16 v[34:37], v[42:45], v[216:219], v[34:37]
	ds_read_b128 v[42:45], v111 offset:256
	ds_read_b128 v[208:211], v111 offset:16640
	ds_read_b128 v[212:215], v111 offset:33024
	ds_read_b128 v[216:219], v111 offset:49408
	s_add_i32 s8, s22, 0xfffa0000
	s_waitcnt vmcnt(17) lgkmcnt(4)
	v_mfma_f32_16x16x32_f16 v[164:167], v[86:89], v[38:41], v[164:167]
	v_mfma_f32_16x16x32_f16 v[168:171], v[86:89], v[156:159], v[168:171]
	v_mfma_f32_16x16x32_f16 v[172:175], v[86:89], v[160:163], v[172:175]
	v_mfma_f32_16x16x32_f16 v[82:85], v[86:89], v[228:231], v[82:85]
	v_mfma_f32_16x16x32_f16 v[58:61], v[74:77], v[38:41], v[58:61]
	v_mfma_f32_16x16x32_f16 v[86:89], v[74:77], v[156:159], v[94:97]
	v_mfma_f32_16x16x32_f16 v[94:97], v[74:77], v[160:163], v[176:179]
	v_mfma_f32_16x16x32_f16 v[70:73], v[74:77], v[228:231], v[70:73]
	v_mfma_f32_16x16x32_f16 v[54:57], v[66:69], v[38:41], v[54:57]
	v_mfma_f32_16x16x32_f16 v[74:77], v[66:69], v[156:159], v[90:93]
	v_mfma_f32_16x16x32_f16 v[90:93], v[66:69], v[160:163], v[180:183]
	v_mfma_f32_16x16x32_f16 v[62:65], v[66:69], v[228:231], v[62:65]
	v_mfma_f32_16x16x32_f16 v[38:41], v[46:49], v[38:41], v[50:53]
	v_mfma_f32_16x16x32_f16 v[50:53], v[46:49], v[156:159], v[78:81]
	v_mfma_f32_16x16x32_f16 v[66:69], v[46:49], v[160:163], v[122:125]
	s_nop 1
	buffer_load_dwordx4 v[78:81], v147, s[16:19], s8 offen
	buffer_load_dwordx4 v[122:125], v148, s[16:19], s8 offen
	buffer_load_dwordx4 v[156:159], v149, s[16:19], s8 offen
	buffer_load_dwordx4 v[160:163], v150, s[16:19], s8 offen
	v_mfma_f32_16x16x32_f16 v[34:37], v[46:49], v[228:231], v[34:37]
	ds_read_b128 v[46:49], v98 offset:256
	ds_read_b128 v[176:179], v98 offset:16640
	ds_read_b128 v[180:183], v98 offset:33024
	ds_read_b128 v[228:231], v98 offset:49408
	s_add_i32 s8, s22, 0xfffa8000
	s_waitcnt vmcnt(17) lgkmcnt(4)
	v_mfma_f32_16x16x32_f16 v[164:167], v[192:195], v[42:45], v[164:167]
	v_mfma_f32_16x16x32_f16 v[168:171], v[192:195], v[208:211], v[168:171]
	v_mfma_f32_16x16x32_f16 v[172:175], v[192:195], v[212:215], v[172:175]
	v_mfma_f32_16x16x32_f16 v[82:85], v[192:195], v[216:219], v[82:85]
	v_mfma_f32_16x16x32_f16 v[58:61], v[196:199], v[42:45], v[58:61]
	v_mfma_f32_16x16x32_f16 v[86:89], v[196:199], v[208:211], v[86:89]
	v_mfma_f32_16x16x32_f16 v[94:97], v[196:199], v[212:215], v[94:97]
	v_mfma_f32_16x16x32_f16 v[70:73], v[196:199], v[216:219], v[70:73]
	v_mfma_f32_16x16x32_f16 v[54:57], v[200:203], v[42:45], v[54:57]
	v_mfma_f32_16x16x32_f16 v[74:77], v[200:203], v[208:211], v[74:77]
	v_mfma_f32_16x16x32_f16 v[90:93], v[200:203], v[212:215], v[90:93]
	v_mfma_f32_16x16x32_f16 v[62:65], v[200:203], v[216:219], v[62:65]
	v_mfma_f32_16x16x32_f16 v[38:41], v[204:207], v[42:45], v[38:41]
	v_mfma_f32_16x16x32_f16 v[42:45], v[204:207], v[208:211], v[50:53]
	v_mfma_f32_16x16x32_f16 v[50:53], v[204:207], v[212:215], v[66:69]
	s_nop 2
	buffer_load_dwordx4 v[66:69], v147, s[16:19], s8 offen
	buffer_load_dwordx4 v[192:195], v148, s[16:19], s8 offen
	buffer_load_dwordx4 v[196:199], v149, s[16:19], s8 offen
	buffer_load_dwordx4 v[200:203], v150, s[16:19], s8 offen
	v_mfma_f32_16x16x32_f16 v[34:37], v[204:207], v[216:219], v[34:37]
	ds_read_b128 v[204:207], v99 offset:256
	ds_read_b128 v[208:211], v99 offset:16640
	ds_read_b128 v[212:215], v99 offset:33024
	ds_read_b128 v[216:219], v99 offset:49408
	s_add_i32 s8, s22, 0xfffb0000
	s_waitcnt vmcnt(17) lgkmcnt(4)
	v_mfma_f32_16x16x32_f16 v[164:167], v[140:143], v[46:49], v[164:167]
	v_mfma_f32_16x16x32_f16 v[168:171], v[140:143], v[176:179], v[168:171]
	v_mfma_f32_16x16x32_f16 v[172:175], v[140:143], v[180:183], v[172:175]
	v_mfma_f32_16x16x32_f16 v[82:85], v[140:143], v[228:231], v[82:85]
	v_mfma_f32_16x16x32_f16 v[58:61], v[220:223], v[46:49], v[58:61]
	v_mfma_f32_16x16x32_f16 v[86:89], v[220:223], v[176:179], v[86:89]
	v_mfma_f32_16x16x32_f16 v[54:57], v[152:155], v[46:49], v[54:57]
	v_mfma_f32_16x16x32_f16 v[74:77], v[152:155], v[176:179], v[74:77]
	v_mfma_f32_16x16x32_f16 v[90:93], v[152:155], v[180:183], v[90:93]
	v_mfma_f32_16x16x32_f16 v[62:65], v[152:155], v[228:231], v[62:65]
	v_mfma_f32_16x16x32_f16 v[38:41], v[224:227], v[46:49], v[38:41]
	v_mfma_f32_16x16x32_f16 v[42:45], v[224:227], v[176:179], v[42:45]
	v_mfma_f32_16x16x32_f16 v[46:49], v[224:227], v[180:183], v[50:53]
	s_nop 2
	buffer_load_dwordx4 v[50:53], v147, s[16:19], s8 offen
	buffer_load_dwordx4 v[140:143], v148, s[16:19], s8 offen
	buffer_load_dwordx4 v[152:155], v149, s[16:19], s8 offen
	buffer_load_dwordx4 v[176:179], v150, s[16:19], s8 offen
	v_mfma_f32_16x16x32_f16 v[94:97], v[220:223], v[180:183], v[94:97]
	v_mfma_f32_16x16x32_f16 v[70:73], v[220:223], v[228:231], v[70:73]
	v_mfma_f32_16x16x32_f16 v[34:37], v[224:227], v[228:231], v[34:37]
	ds_read_b128 v[180:183], v100 offset:256
	ds_read_b128 v[220:223], v100 offset:16640
	ds_read_b128 v[224:227], v100 offset:33024
	ds_read_b128 v[228:231], v100 offset:49408
	s_add_i32 s8, s22, 0xfffb8000
	s_waitcnt vmcnt(12) lgkmcnt(4)
	v_mfma_f32_16x16x32_f16 v[164:167], v[126:129], v[204:207], v[164:167]
	v_mfma_f32_16x16x32_f16 v[168:171], v[126:129], v[208:211], v[168:171]
	v_mfma_f32_16x16x32_f16 v[172:175], v[126:129], v[212:215], v[172:175]
	v_mfma_f32_16x16x32_f16 v[82:85], v[126:129], v[216:219], v[82:85]
	v_mfma_f32_16x16x32_f16 v[58:61], v[136:139], v[204:207], v[58:61]
	v_mfma_f32_16x16x32_f16 v[86:89], v[136:139], v[208:211], v[86:89]
	v_mfma_f32_16x16x32_f16 v[94:97], v[136:139], v[212:215], v[94:97]
	v_mfma_f32_16x16x32_f16 v[70:73], v[136:139], v[216:219], v[70:73]
	v_mfma_f32_16x16x32_f16 v[54:57], v[184:187], v[204:207], v[54:57]
	v_mfma_f32_16x16x32_f16 v[74:77], v[184:187], v[208:211], v[74:77]
	v_mfma_f32_16x16x32_f16 v[90:93], v[184:187], v[212:215], v[90:93]
	v_mfma_f32_16x16x32_f16 v[62:65], v[184:187], v[216:219], v[62:65]
	v_mfma_f32_16x16x32_f16 v[38:41], v[188:191], v[204:207], v[38:41]
	buffer_load_dwordx4 v[126:129], v147, s[16:19], s8 offen
	buffer_load_dwordx4 v[136:139], v148, s[16:19], s8 offen
	buffer_load_dwordx4 v[184:187], v149, s[16:19], s8 offen
	buffer_load_dwordx4 v[204:207], v150, s[16:19], s8 offen
	v_mfma_f32_16x16x32_f16 v[42:45], v[188:191], v[208:211], v[42:45]
	v_mfma_f32_16x16x32_f16 v[46:49], v[188:191], v[212:215], v[46:49]
	v_mfma_f32_16x16x32_f16 v[34:37], v[188:191], v[216:219], v[34:37]
	ds_read_b128 v[188:191], v111 offset:512
	ds_read_b128 v[208:211], v111 offset:16896
	ds_read_b128 v[212:215], v111 offset:33280
	ds_read_b128 v[216:219], v111 offset:49664
	s_add_i32 s8, s22, 0xfffc0000
	s_waitcnt vmcnt(12) lgkmcnt(4)
	v_mfma_f32_16x16x32_f16 v[164:167], v[78:81], v[180:183], v[164:167]
	v_mfma_f32_16x16x32_f16 v[168:171], v[78:81], v[220:223], v[168:171]
	v_mfma_f32_16x16x32_f16 v[172:175], v[78:81], v[224:227], v[172:175]
	v_mfma_f32_16x16x32_f16 v[78:81], v[78:81], v[228:231], v[82:85]
	v_mfma_f32_16x16x32_f16 v[58:61], v[122:125], v[180:183], v[58:61]
	v_mfma_f32_16x16x32_f16 v[82:85], v[122:125], v[220:223], v[86:89]
	v_mfma_f32_16x16x32_f16 v[86:89], v[122:125], v[224:227], v[94:97]
	v_mfma_f32_16x16x32_f16 v[70:73], v[122:125], v[228:231], v[70:73]
	v_mfma_f32_16x16x32_f16 v[54:57], v[156:159], v[180:183], v[54:57]
	v_mfma_f32_16x16x32_f16 v[74:77], v[156:159], v[220:223], v[74:77]
	v_mfma_f32_16x16x32_f16 v[90:93], v[156:159], v[224:227], v[90:93]
	v_mfma_f32_16x16x32_f16 v[62:65], v[156:159], v[228:231], v[62:65]
	v_mfma_f32_16x16x32_f16 v[38:41], v[160:163], v[180:183], v[38:41]
	buffer_load_dwordx4 v[94:97], v147, s[16:19], s8 offen
	buffer_load_dwordx4 v[122:125], v148, s[16:19], s8 offen
	buffer_load_dwordx4 v[156:159], v149, s[16:19], s8 offen
	buffer_load_dwordx4 v[180:183], v150, s[16:19], s8 offen
	v_mfma_f32_16x16x32_f16 v[42:45], v[160:163], v[220:223], v[42:45]
	v_mfma_f32_16x16x32_f16 v[46:49], v[160:163], v[224:227], v[46:49]
	v_mfma_f32_16x16x32_f16 v[34:37], v[160:163], v[228:231], v[34:37]
	ds_read_b128 v[160:163], v98 offset:512
	ds_read_b128 v[220:223], v98 offset:16896
	ds_read_b128 v[224:227], v98 offset:33280
	ds_read_b128 v[228:231], v98 offset:49664
	s_add_i32 s8, s22, 0xfffc8000
	s_waitcnt vmcnt(12) lgkmcnt(4)
	v_mfma_f32_16x16x32_f16 v[164:167], v[66:69], v[188:191], v[164:167]
	v_mfma_f32_16x16x32_f16 v[168:171], v[66:69], v[208:211], v[168:171]
	v_mfma_f32_16x16x32_f16 v[172:175], v[66:69], v[212:215], v[172:175]
	v_mfma_f32_16x16x32_f16 v[66:69], v[66:69], v[216:219], v[78:81]
	v_mfma_f32_16x16x32_f16 v[58:61], v[192:195], v[188:191], v[58:61]
	v_mfma_f32_16x16x32_f16 v[78:81], v[192:195], v[208:211], v[82:85]
	v_mfma_f32_16x16x32_f16 v[82:85], v[192:195], v[212:215], v[86:89]
	v_mfma_f32_16x16x32_f16 v[70:73], v[192:195], v[216:219], v[70:73]
	v_mfma_f32_16x16x32_f16 v[54:57], v[196:199], v[188:191], v[54:57]
	v_mfma_f32_16x16x32_f16 v[74:77], v[196:199], v[208:211], v[74:77]
	v_mfma_f32_16x16x32_f16 v[86:89], v[196:199], v[212:215], v[90:93]
	v_mfma_f32_16x16x32_f16 v[62:65], v[196:199], v[216:219], v[62:65]
	v_mfma_f32_16x16x32_f16 v[38:41], v[200:203], v[188:191], v[38:41]
	buffer_load_dwordx4 v[90:93], v147, s[16:19], s8 offen
	buffer_load_dwordx4 v[188:191], v148, s[16:19], s8 offen
	buffer_load_dwordx4 v[192:195], v149, s[16:19], s8 offen
	buffer_load_dwordx4 v[196:199], v150, s[16:19], s8 offen
	v_mfma_f32_16x16x32_f16 v[42:45], v[200:203], v[208:211], v[42:45]
	v_mfma_f32_16x16x32_f16 v[46:49], v[200:203], v[212:215], v[46:49]
	v_mfma_f32_16x16x32_f16 v[34:37], v[200:203], v[216:219], v[34:37]
	ds_read_b128 v[200:203], v99 offset:512
	ds_read_b128 v[208:211], v99 offset:16896
	ds_read_b128 v[212:215], v99 offset:33280
	ds_read_b128 v[216:219], v99 offset:49664
	s_add_i32 s8, s22, 0xfffd0000
	s_waitcnt vmcnt(12) lgkmcnt(4)
	v_mfma_f32_16x16x32_f16 v[164:167], v[50:53], v[160:163], v[164:167]
	v_mfma_f32_16x16x32_f16 v[168:171], v[50:53], v[220:223], v[168:171]
	v_mfma_f32_16x16x32_f16 v[172:175], v[50:53], v[224:227], v[172:175]
	v_mfma_f32_16x16x32_f16 v[50:53], v[50:53], v[228:231], v[66:69]
	v_mfma_f32_16x16x32_f16 v[58:61], v[140:143], v[160:163], v[58:61]
	v_mfma_f32_16x16x32_f16 v[66:69], v[140:143], v[220:223], v[78:81]
	v_mfma_f32_16x16x32_f16 v[78:81], v[140:143], v[224:227], v[82:85]
	v_mfma_f32_16x16x32_f16 v[70:73], v[140:143], v[228:231], v[70:73]
	v_mfma_f32_16x16x32_f16 v[54:57], v[152:155], v[160:163], v[54:57]
	v_mfma_f32_16x16x32_f16 v[74:77], v[152:155], v[220:223], v[74:77]
	v_mfma_f32_16x16x32_f16 v[82:85], v[152:155], v[224:227], v[86:89]
	v_mfma_f32_16x16x32_f16 v[62:65], v[152:155], v[228:231], v[62:65]
	v_mfma_f32_16x16x32_f16 v[38:41], v[176:179], v[160:163], v[38:41]
	buffer_load_dwordx4 v[86:89], v147, s[16:19], s8 offen
	buffer_load_dwordx4 v[140:143], v148, s[16:19], s8 offen
	buffer_load_dwordx4 v[152:155], v149, s[16:19], s8 offen
	buffer_load_dwordx4 v[160:163], v150, s[16:19], s8 offen
	v_mfma_f32_16x16x32_f16 v[42:45], v[176:179], v[220:223], v[42:45]
	v_mfma_f32_16x16x32_f16 v[46:49], v[176:179], v[224:227], v[46:49]
	v_mfma_f32_16x16x32_f16 v[34:37], v[176:179], v[228:231], v[34:37]
	ds_read_b128 v[176:179], v100 offset:512
	ds_read_b128 v[220:223], v100 offset:16896
	ds_read_b128 v[224:227], v100 offset:33280
	ds_read_b128 v[228:231], v100 offset:49664
	s_add_i32 s8, s22, 0xfffd8000
	s_waitcnt vmcnt(12) lgkmcnt(4)
	v_mfma_f32_16x16x32_f16 v[164:167], v[126:129], v[200:203], v[164:167]
	v_mfma_f32_16x16x32_f16 v[168:171], v[126:129], v[208:211], v[168:171]
	v_mfma_f32_16x16x32_f16 v[172:175], v[126:129], v[212:215], v[172:175]
	v_mfma_f32_16x16x32_f16 v[50:53], v[126:129], v[216:219], v[50:53]
	v_mfma_f32_16x16x32_f16 v[58:61], v[136:139], v[200:203], v[58:61]
	v_mfma_f32_16x16x32_f16 v[66:69], v[136:139], v[208:211], v[66:69]
	v_mfma_f32_16x16x32_f16 v[78:81], v[136:139], v[212:215], v[78:81]
	v_mfma_f32_16x16x32_f16 v[70:73], v[136:139], v[216:219], v[70:73]
	v_mfma_f32_16x16x32_f16 v[54:57], v[184:187], v[200:203], v[54:57]
	v_mfma_f32_16x16x32_f16 v[74:77], v[184:187], v[208:211], v[74:77]
	v_mfma_f32_16x16x32_f16 v[82:85], v[184:187], v[212:215], v[82:85]
	v_mfma_f32_16x16x32_f16 v[62:65], v[184:187], v[216:219], v[62:65]
	v_mfma_f32_16x16x32_f16 v[38:41], v[204:207], v[200:203], v[38:41]
	buffer_load_dwordx4 v[126:129], v147, s[16:19], s8 offen
	buffer_load_dwordx4 v[136:139], v148, s[16:19], s8 offen
	buffer_load_dwordx4 v[184:187], v149, s[16:19], s8 offen
	buffer_load_dwordx4 v[200:203], v150, s[16:19], s8 offen
	v_mfma_f32_16x16x32_f16 v[42:45], v[204:207], v[208:211], v[42:45]
	v_mfma_f32_16x16x32_f16 v[46:49], v[204:207], v[212:215], v[46:49]
	v_mfma_f32_16x16x32_f16 v[34:37], v[204:207], v[216:219], v[34:37]
	ds_read_b128 v[204:207], v111 offset:768
	ds_read_b128 v[208:211], v111 offset:17152
	ds_read_b128 v[212:215], v111 offset:33536
	ds_read_b128 v[216:219], v111 offset:49920
	s_add_i32 s8, s22, 0xfffe0000
	s_waitcnt vmcnt(12) lgkmcnt(4)
	v_mfma_f32_16x16x32_f16 v[164:167], v[94:97], v[176:179], v[164:167]
	v_mfma_f32_16x16x32_f16 v[168:171], v[94:97], v[220:223], v[168:171]
	v_mfma_f32_16x16x32_f16 v[58:61], v[122:125], v[176:179], v[58:61]
	v_mfma_f32_16x16x32_f16 v[66:69], v[122:125], v[220:223], v[66:69]
	v_mfma_f32_16x16x32_f16 v[78:81], v[122:125], v[224:227], v[78:81]
	v_mfma_f32_16x16x32_f16 v[70:73], v[122:125], v[228:231], v[70:73]
	v_mfma_f32_16x16x32_f16 v[54:57], v[156:159], v[176:179], v[54:57]
	v_mfma_f32_16x16x32_f16 v[74:77], v[156:159], v[220:223], v[74:77]
	v_mfma_f32_16x16x32_f16 v[82:85], v[156:159], v[224:227], v[82:85]
	v_mfma_f32_16x16x32_f16 v[62:65], v[156:159], v[228:231], v[62:65]
	v_mfma_f32_16x16x32_f16 v[38:41], v[180:183], v[176:179], v[38:41]
	v_mfma_f32_16x16x32_f16 v[42:45], v[180:183], v[220:223], v[42:45]
	buffer_load_dwordx4 v[122:125], v147, s[16:19], s8 offen
	buffer_load_dwordx4 v[156:159], v148, s[16:19], s8 offen
	buffer_load_dwordx4 v[176:179], v149, s[16:19], s8 offen
	buffer_load_dwordx4 v[220:223], v150, s[16:19], s8 offen
	v_mfma_f32_16x16x32_f16 v[50:53], v[94:97], v[228:231], v[50:53]
	v_mfma_f32_16x16x32_f16 v[46:49], v[180:183], v[224:227], v[46:49]
	v_mfma_f32_16x16x32_f16 v[34:37], v[180:183], v[228:231], v[34:37]
	v_mfma_f32_16x16x32_f16 v[172:175], v[94:97], v[224:227], v[172:175]
	ds_read_b128 v[94:97], v98 offset:768
	ds_read_b128 v[180:183], v98 offset:17152
	ds_read_b128 v[224:227], v98 offset:33536
	ds_read_b128 v[228:231], v98 offset:49920
	s_add_i32 s8, s22, 0xfffe8000
	s_waitcnt vmcnt(12) lgkmcnt(4)
	v_mfma_f32_16x16x32_f16 v[164:167], v[90:93], v[204:207], v[164:167]
	v_mfma_f32_16x16x32_f16 v[168:171], v[90:93], v[208:211], v[168:171]
	v_mfma_f32_16x16x32_f16 v[172:175], v[90:93], v[212:215], v[172:175]
	v_mfma_f32_16x16x32_f16 v[90:93], v[90:93], v[216:219], v[50:53]
	v_mfma_f32_16x16x32_f16 v[232:235], v[188:191], v[204:207], v[58:61]
	v_mfma_f32_16x16x32_f16 v[66:69], v[188:191], v[208:211], v[66:69]
	v_mfma_f32_16x16x32_f16 v[78:81], v[188:191], v[212:215], v[78:81]
	v_mfma_f32_16x16x32_f16 v[70:73], v[188:191], v[216:219], v[70:73]
	v_mfma_f32_16x16x32_f16 v[188:191], v[192:195], v[204:207], v[54:57]
	v_mfma_f32_16x16x32_f16 v[74:77], v[192:195], v[208:211], v[74:77]
	v_mfma_f32_16x16x32_f16 v[82:85], v[192:195], v[212:215], v[82:85]
	v_mfma_f32_16x16x32_f16 v[62:65], v[192:195], v[216:219], v[62:65]
	v_mfma_f32_16x16x32_f16 v[192:195], v[196:199], v[204:207], v[38:41]
	buffer_load_dwordx4 v[58:61], v147, s[16:19], s8 offen
	buffer_load_dwordx4 v[54:57], v148, s[16:19], s8 offen
	buffer_load_dwordx4 v[50:53], v149, s[16:19], s8 offen
	buffer_load_dwordx4 v[38:41], v150, s[16:19], s8 offen
	v_mfma_f32_16x16x32_f16 v[42:45], v[196:199], v[208:211], v[42:45]
	v_mfma_f32_16x16x32_f16 v[46:49], v[196:199], v[212:215], v[46:49]
	v_mfma_f32_16x16x32_f16 v[196:199], v[196:199], v[216:219], v[34:37]
	ds_read_b128 v[204:207], v99 offset:768
	ds_read_b128 v[208:211], v99 offset:17152
	ds_read_b128 v[212:215], v99 offset:33536
	ds_read_b128 v[216:219], v99 offset:49920
	s_add_i32 s8, s22, 0xffff0000
	s_waitcnt vmcnt(12) lgkmcnt(4)
	v_mfma_f32_16x16x32_f16 v[164:167], v[86:89], v[94:97], v[164:167]
	v_mfma_f32_16x16x32_f16 v[168:171], v[86:89], v[180:183], v[168:171]
	v_mfma_f32_16x16x32_f16 v[172:175], v[86:89], v[224:227], v[172:175]
	v_mfma_f32_16x16x32_f16 v[86:89], v[86:89], v[228:231], v[90:93]
	v_mfma_f32_16x16x32_f16 v[232:235], v[140:143], v[94:97], v[232:235]
	v_mfma_f32_16x16x32_f16 v[66:69], v[140:143], v[180:183], v[66:69]
	v_mfma_f32_16x16x32_f16 v[236:239], v[140:143], v[224:227], v[78:81]
	v_mfma_f32_16x16x32_f16 v[70:73], v[140:143], v[228:231], v[70:73]
	v_mfma_f32_16x16x32_f16 v[140:143], v[152:155], v[94:97], v[188:191]
	v_mfma_f32_16x16x32_f16 v[74:77], v[152:155], v[180:183], v[74:77]
	v_mfma_f32_16x16x32_f16 v[82:85], v[152:155], v[224:227], v[82:85]
	v_mfma_f32_16x16x32_f16 v[62:65], v[152:155], v[228:231], v[62:65]
	v_mfma_f32_16x16x32_f16 v[152:155], v[160:163], v[94:97], v[192:195]
	buffer_load_dwordx4 v[94:97], v147, s[16:19], s8 offen
	buffer_load_dwordx4 v[90:93], v148, s[16:19], s8 offen
	buffer_load_dwordx4 v[78:81], v149, s[16:19], s8 offen
	buffer_load_dwordx4 v[34:37], v150, s[16:19], s8 offen
	v_mfma_f32_16x16x32_f16 v[42:45], v[160:163], v[180:183], v[42:45]
	v_mfma_f32_16x16x32_f16 v[46:49], v[160:163], v[224:227], v[46:49]
	v_mfma_f32_16x16x32_f16 v[160:163], v[160:163], v[228:231], v[196:199]
	ds_read_b128 v[180:183], v100 offset:768
	ds_read_b128 v[188:191], v100 offset:17152
	ds_read_b128 v[192:195], v100 offset:33536
	ds_read_b128 v[196:199], v100 offset:49920
	s_add_i32 s8, s22, 0xffff8000
	s_waitcnt vmcnt(12) lgkmcnt(4)
	v_mfma_f32_16x16x32_f16 v[164:167], v[126:129], v[204:207], v[164:167]
	v_mfma_f32_16x16x32_f16 v[168:171], v[126:129], v[208:211], v[168:171]
	v_mfma_f32_16x16x32_f16 v[172:175], v[126:129], v[212:215], v[172:175]
	v_mfma_f32_16x16x32_f16 v[86:89], v[126:129], v[216:219], v[86:89]
	v_mfma_f32_16x16x32_f16 v[126:129], v[136:139], v[204:207], v[232:235]
	v_mfma_f32_16x16x32_f16 v[66:69], v[136:139], v[208:211], v[66:69]
	v_mfma_f32_16x16x32_f16 v[224:227], v[136:139], v[212:215], v[236:239]
	v_mfma_f32_16x16x32_f16 v[136:139], v[136:139], v[216:219], v[70:73]
	v_mfma_f32_16x16x32_f16 v[140:143], v[184:187], v[204:207], v[140:143]
	v_mfma_f32_16x16x32_f16 v[74:77], v[184:187], v[208:211], v[74:77]
	v_mfma_f32_16x16x32_f16 v[228:231], v[184:187], v[212:215], v[82:85]
	v_mfma_f32_16x16x32_f16 v[184:187], v[184:187], v[216:219], v[62:65]
	v_mfma_f32_16x16x32_f16 v[152:155], v[200:203], v[204:207], v[152:155]
	v_mfma_f32_16x16x32_f16 v[204:207], v[200:203], v[208:211], v[42:45]
	buffer_load_dwordx4 v[82:85], v147, s[16:19], s8 offen
	buffer_load_dwordx4 v[70:73], v148, s[16:19], s8 offen
	buffer_load_dwordx4 v[62:65], v149, s[16:19], s8 offen
	buffer_load_dwordx4 v[42:45], v150, s[16:19], s8 offen
	v_mfma_f32_16x16x32_f16 v[46:49], v[200:203], v[212:215], v[46:49]
	v_mfma_f32_16x16x32_f16 v[160:163], v[200:203], v[216:219], v[160:163]
	v_add_u32_e32 v0, 0x1ac00, v104
	ds_read_b128 v[240:243], v0
	ds_read_b128 v[244:247], v0 offset:16
	s_waitcnt vmcnt(12) lgkmcnt(5)
	v_mfma_f32_16x16x32_f16 v[164:167], v[122:125], v[180:183], v[164:167]
	v_mfma_f32_16x16x32_f16 v[126:129], v[156:159], v[180:183], v[126:129]
	v_mfma_f32_16x16x32_f16 v[140:143], v[176:179], v[180:183], v[140:143]
	v_mfma_f32_16x16x32_f16 v[152:155], v[220:223], v[180:183], v[152:155]
	s_waitcnt lgkmcnt(4)
	v_mfma_f32_16x16x32_f16 v[168:171], v[122:125], v[188:191], v[168:171]
	v_mfma_f32_16x16x32_f16 v[208:211], v[156:159], v[188:191], v[66:69]
	v_mfma_f32_16x16x32_f16 v[212:215], v[176:179], v[188:191], v[74:77]
	v_mfma_f32_16x16x32_f16 v[204:207], v[220:223], v[188:191], v[204:207]
	s_waitcnt lgkmcnt(3)
	v_mfma_f32_16x16x32_f16 v[172:175], v[122:125], v[192:195], v[172:175]
	v_cvt_pk_f16_f32 v232, v164, v165
	v_cvt_pk_f16_f32 v233, v166, v167
	v_pk_max_f16 v232, v232, 0
	v_pk_max_f16 v233, v233, 0
	v_mfma_f32_16x16x32_f16 v[224:227], v[156:159], v[192:195], v[224:227]
	v_cvt_pk_f16_f32 v234, v126, v127
	v_cvt_pk_f16_f32 v235, v128, v129
	v_pk_max_f16 v234, v234, 0
	v_pk_max_f16 v235, v235, 0
	v_mfma_f32_16x16x32_f16 v[228:231], v[176:179], v[192:195], v[228:231]
	v_cvt_pk_f16_f32 v236, v140, v141
	v_cvt_pk_f16_f32 v237, v142, v143
	v_pk_max_f16 v236, v236, 0
	v_pk_max_f16 v237, v237, 0
	v_mfma_f32_16x16x32_f16 v[216:219], v[220:223], v[192:195], v[46:49]
	v_cvt_pk_f16_f32 v238, v152, v153
	v_cvt_pk_f16_f32 v239, v154, v155
	v_pk_max_f16 v238, v238, 0
	v_pk_max_f16 v239, v239, 0
	s_waitcnt lgkmcnt(2)
	v_mfma_f32_16x16x32_f16 v[200:203], v[122:125], v[196:199], v[86:89]
	v_cvt_pk_f16_f32 v180, v168, v169
	v_cvt_pk_f16_f32 v181, v170, v171
	v_pk_max_f16 v180, v180, 0
	v_pk_max_f16 v181, v181, 0
	buffer_load_dwordx4 v[86:89], v147, s[16:19], s22 offen
	buffer_load_dwordx4 v[74:77], v148, s[16:19], s22 offen
	buffer_load_dwordx4 v[66:69], v149, s[16:19], s22 offen
	buffer_load_dwordx4 v[46:49], v150, s[16:19], s22 offen
	v_mfma_f32_16x16x32_f16 v[136:139], v[156:159], v[196:199], v[136:139]
	v_cvt_pk_f16_f32 v182, v208, v209
	v_cvt_pk_f16_f32 v183, v210, v211
	v_pk_max_f16 v182, v182, 0
	v_pk_max_f16 v183, v183, 0
	s_waitcnt lgkmcnt(1)
	v_mfma_f32_16x16x32_f16 v[252:255], v[240:243], v[232:235], 0
	v_mfma_f32_16x16x32_f16 v[184:187], v[176:179], v[196:199], v[184:187]
	v_cvt_pk_f16_f32 v188, v212, v213
	v_cvt_pk_f16_f32 v189, v214, v215
	v_pk_max_f16 v188, v188, 0
	v_pk_max_f16 v189, v189, 0
	s_waitcnt lgkmcnt(0)
	v_mfma_f32_16x16x32_f16 v[252:255], v[244:247], v[236:239], v[252:255]
	v_mfma_f32_16x16x32_f16 v[160:163], v[220:223], v[196:199], v[160:163]
	v_cvt_pk_f16_f32 v190, v204, v205
	v_cvt_pk_f16_f32 v191, v206, v207
	v_pk_max_f16 v190, v190, 0
	v_pk_max_f16 v191, v191, 0
	v_cvt_pk_f16_f32 v232, v172, v173
	v_cvt_pk_f16_f32 v233, v174, v175
	v_pk_max_f16 v232, v232, 0
	v_pk_max_f16 v233, v233, 0
	v_cvt_pk_f16_f32 v234, v224, v225
	v_cvt_pk_f16_f32 v235, v226, v227
	v_pk_max_f16 v234, v234, 0
	v_pk_max_f16 v235, v235, 0
	v_mfma_f32_16x16x32_f16 v[192:195], v[240:243], v[180:183], 0
	v_cvt_pk_f16_f32 v236, v228, v229
	v_cvt_pk_f16_f32 v237, v230, v231
	v_pk_max_f16 v236, v236, 0
	v_pk_max_f16 v237, v237, 0
	v_mfma_f32_16x16x32_f16 v[192:195], v[244:247], v[188:191], v[192:195]
	v_cvt_pk_f16_f32 v238, v216, v217
	v_cvt_pk_f16_f32 v239, v218, v219
	v_pk_max_f16 v238, v238, 0
	v_pk_max_f16 v239, v239, 0
	v_cvt_pk_f16_f32 v180, v200, v201
	v_cvt_pk_f16_f32 v181, v202, v203
	v_pk_max_f16 v180, v180, 0
	v_pk_max_f16 v181, v181, 0
	v_mfma_f32_16x16x32_f16 v[196:199], v[240:243], v[232:235], 0
	v_cvt_pk_f16_f32 v182, v136, v137
	v_cvt_pk_f16_f32 v183, v138, v139
	v_pk_max_f16 v182, v182, 0
	v_pk_max_f16 v183, v183, 0
	v_mfma_f32_16x16x32_f16 v[196:199], v[244:247], v[236:239], v[196:199]
	v_cvt_pk_f16_f32 v188, v184, v185
	v_cvt_pk_f16_f32 v189, v186, v187
	v_pk_max_f16 v188, v188, 0
	v_pk_max_f16 v189, v189, 0
	v_cvt_pk_f16_f32 v190, v160, v161
	v_cvt_pk_f16_f32 v191, v162, v163
	v_pk_max_f16 v190, v190, 0
	v_pk_max_f16 v191, v191, 0
	v_mfma_f32_16x16x32_f16 v[122:125], v[240:243], v[180:183], 0
	s_nop 0
	v_mfma_f32_16x16x32_f16 v[122:125], v[244:247], v[188:191], v[122:125]
	s_load_dword s30, s[12:13], 0x0
	v_cndmask_b32_e64 v0, v252, v192, s[2:3]
	v_cndmask_b32_e64 v0, v0, v196, s[0:1]
	s_waitcnt vmcnt(16)
	v_cndmask_b32_e64 v1, v30, v134, s[0:1]
	v_bfi_b32 v30, s10, v1, v30
	v_perm_b32 v1, v22, v134, s24
	v_cndmask_b32_e64 v22, v22, v1, s[0:1]
	v_bfi_b32 v1, s10, v135, v18
	v_perm_b32 v121, v10, v135, s24
	v_cndmask_b32_e64 v18, v18, v1, s[0:1]
	v_cndmask_b32_e64 v10, v10, v121, s[0:1]
	v_cndmask_b32_e64 v0, v0, v122, s[26:27]
	ds_write_b32 v112, v0
	s_waitcnt lgkmcnt(0)
	s_barrier
	ds_read_b128 v[232:235], v113
	ds_read_b128 v[236:239], v113 offset:1024
	ds_read_u16 v248, v114
	ds_read_u16 v249, v114 offset:512
	ds_read_u16 v250, v114 offset:1024
	ds_read_u16 v251, v114 offset:1536
	s_and_b64 vcc, exec, s[4:5]
	s_waitcnt lgkmcnt(4)
	v_add_f32_e32 v0, v232, v233
	v_add_f32_e32 v1, v234, v235
	v_add_f32_e32 v121, v236, v237
	v_add_f32_e32 v144, v238, v239
	v_add_f32_e32 v0, v0, v1
	v_add_f32_e32 v121, v121, v144
	v_add_f32_e32 v0, v0, v121
	v_add_f32_e32 v0, s30, v0
	s_cbranch_vccnz .Lskip_out
	ds_write_b32 v106, v0
